# post-MFMA VALU trims: window zero-adds folded and one v_max instead of three; cmp quad reduction uses two DPP adds, rescale threshold kept in a register
# speedup vs baseline: 1.0033x; 1.0008x over previous
; #define SBAR() __builtin_amdgcn_sched_barrier(0)
; __device__ __forceinline__ u32x4 pack8f(const f32x4 a, const f32x4 b) { u32x4 w; w.x = pk2(a[0], a[1]); w.y = pk2(a[2], a[3]); w.z = pk2(b[0], b[1]); w.w = pk2(b[2], b[3]); return w; }
; #define PV_RD(dt) do { TRRD(r[dt][0], vb, (dt) * 32); TRRD(r[dt][1], vb, (dt) * 32 + 4608); TRRD(r[dt][2], vb, (dt) * 32 + 9216); TRRD(r[dt][3], vb, (dt) * 32 + 9216 + 4608); } while (0)
; #define PV_W(n) asm volatile("s_waitcnt lgkmcnt(" #n ")" ::: "memory"); SBAR()
; template <bool WITH_O, class G> __device__ __forceinline__ void online_smc(f32x4 (&s)[4], G& g, const float ref) {
;     ...
;     float ps = 0.f;
; #pragma unroll
;     for (int T_ = 0; T_ < 4; ++T_)
; #pragma unroll
;         for (int i = 0; i < 4; ++i) { s[T_][i] = __builtin_amdgcn_exp2f(s[T_][i]); ps += s[T_][i]; }
;     g.l += ps;
; }
; __device__ __forceinline__ bf16x8 ppack(const f32x4 a, const f32x4 b) { const u32x4 w = pack8f(a, b); return __builtin_bit_cast(bf16x8, w); }
; template <int NG, class G> __device__ __forceinline__ void pv_tile(G& g0, G& g1, const f32x4 (&s0)[4], const f32x4 (&s1)[4], unsigned vb) {
;     const bf16x8 pa0 = ppack(s0[0], s0[1]), pa1 = ppack(s0[2], s0[3]);
;     bf16x8 pb0 = pa0, pb1 = pa1; if (NG == 2) { pb0 = ppack(s1[0], s1[1]); pb1 = ppack(s1[2], s1[3]); }
;     s16x4 r[8][4];
;     ...
;     PV_RD(0); PV_RD(1); PV_RD(2);
;     __builtin_amdgcn_s_setprio(1);
;     PV_W(8); PV_MM(0); SBAR(); PV_RD(3);
;     PV_W(8); PV_MM(1); SBAR(); PV_RD(4);
;     PV_W(8); PV_MM(2); SBAR(); PV_RD(5);
;     PV_W(8); PV_MM(3); SBAR(); PV_RD(6);
;     PV_W(8); PV_MM(4); SBAR(); PV_RD(7);
;     PV_W(8); PV_MM(5); PV_W(4); PV_MM(6); PV_W(0); PV_MM(7);
;     __builtin_amdgcn_s_setprio(0);
.LBB0_1470:
	v_exp_f32_e32 v100, v100
	v_exp_f32_e32 v101, v101
	v_exp_f32_e32 v102, v102
	v_exp_f32_e32 v103, v103
	v_exp_f32_e32 v108, v108
	v_add_f32_e32 v130, v101, v100
	v_exp_f32_e32 v109, v109
	v_add_f32_e32 v130, v102, v130
	v_exp_f32_e32 v110, v110
	v_add_f32_e32 v130, v103, v130
	v_exp_f32_e32 v111, v111
	v_add_f32_e32 v130, v108, v130
	v_exp_f32_e32 v104, v104
	v_add_f32_e32 v130, v109, v130
	v_exp_f32_e32 v105, v105
	v_add_f32_e32 v130, v110, v130
	v_exp_f32_e32 v106, v106
	v_add_f32_e32 v130, v111, v130
	v_exp_f32_e32 v107, v107
	v_add_f32_e32 v130, v104, v130
	v_exp_f32_e32 v96, v96
	v_add_f32_e32 v130, v105, v130
	v_exp_f32_e32 v97, v97
	v_add_f32_e32 v130, v106, v130
	v_exp_f32_e32 v98, v98
	v_add_f32_e32 v130, v107, v130
	v_exp_f32_e32 v99, v99
	v_add_f32_e32 v130, v96, v130
	v_exp_f32_e32 v92, v92
	v_add_f32_e32 v130, v97, v130
	v_exp_f32_e32 v93, v93
	v_add_f32_e32 v130, v98, v130
	v_exp_f32_e32 v94, v94
	v_add_f32_e32 v130, v99, v130
	v_exp_f32_e32 v95, v95
	v_add_f32_e32 v152, v152, v130
	v_exp_f32_e32 v134, v88
	v_add_f32_e32 v130, v93, v92
	v_exp_f32_e32 v136, v89
	v_add_f32_e32 v130, v94, v130
	v_exp_f32_e32 v138, v90
	v_add_f32_e32 v130, v95, v130
	v_exp_f32_e32 v91, v91
	v_add_f32_e32 v88, v134, v130
	v_exp_f32_e32 v130, v80
	v_add_f32_e32 v88, v136, v88
	v_exp_f32_e32 v139, v81
	v_add_f32_e32 v88, v138, v88
	v_exp_f32_e32 v157, v82
	v_add_f32_e32 v88, v91, v88
	v_exp_f32_e32 v158, v83
	v_add_f32_e32 v80, v130, v88
	v_exp_f32_e32 v159, v84
	v_add_f32_e32 v80, v139, v80
	v_exp_f32_e32 v160, v85
	v_add_f32_e32 v80, v157, v80
	v_exp_f32_e32 v161, v86
	v_add_f32_e32 v80, v158, v80
	v_exp_f32_e32 v162, v87
	v_add_f32_e32 v80, v159, v80
	v_add_f32_e32 v80, v160, v80
	v_add_f32_e32 v80, v161, v80
	v_add_f32_e32 v80, v162, v80
	s_addk_i32 s6, 0x2400
	v_add_f32_e32 v153, v153, v80
	v_add_u32_e32 v166, s6, v142
	v_cvt_pk_bf16_f32 v80, v100, v101
	v_cvt_pk_bf16_f32 v81, v102, v103
	v_cvt_pk_bf16_f32 v82, v108, v109
	v_cvt_pk_bf16_f32 v83, v110, v111
	v_cvt_pk_bf16_f32 v84, v104, v105
	v_cvt_pk_bf16_f32 v85, v106, v107
	v_cvt_pk_bf16_f32 v86, v96, v97
	v_cvt_pk_bf16_f32 v87, v98, v99
	v_cvt_pk_bf16_f32 v88, v92, v93
	v_cvt_pk_bf16_f32 v89, v94, v95
	v_cvt_pk_bf16_f32 v90, v134, v136
	v_cvt_pk_bf16_f32 v91, v138, v91
	v_cvt_pk_bf16_f32 v92, v130, v139
	v_cvt_pk_bf16_f32 v93, v157, v158
	v_cvt_pk_bf16_f32 v94, v159, v160
	v_cvt_pk_bf16_f32 v95, v161, v162
	ds_read_b64_tr_b16 v[96:97], v166 offset:0
	ds_read_b64_tr_b16 v[98:99], v166 offset:0x1200
	ds_read_b64_tr_b16 v[100:101], v166 offset:0x2400
	ds_read_b64_tr_b16 v[102:103], v166 offset:0x3600
	ds_read_b64_tr_b16 v[104:105], v166 offset:32
	ds_read_b64_tr_b16 v[106:107], v166 offset:0x1220
	ds_read_b64_tr_b16 v[108:109], v166 offset:0x2420
	ds_read_b64_tr_b16 v[110:111], v166 offset:0x3620
	ds_read_b64_tr_b16 v[158:159], v166 offset:64
	ds_read_b64_tr_b16 v[160:161], v166 offset:0x1240
	ds_read_b64_tr_b16 v[162:163], v166 offset:0x2440
	ds_read_b64_tr_b16 v[164:165], v166 offset:0x3640
	s_setprio 1
	s_waitcnt lgkmcnt(8)
	v_mfma_f32_16x16x32_bf16 v[48:51], v[96:99], v[80:83], v[48:51]
	v_mfma_f32_16x16x32_bf16 v[16:19], v[96:99], v[88:91], v[16:19]
	v_mfma_f32_16x16x32_bf16 v[48:51], v[100:103], v[84:87], v[48:51]
	v_mfma_f32_16x16x32_bf16 v[16:19], v[100:103], v[92:95], v[16:19]
	ds_read_b64_tr_b16 v[96:97], v166 offset:0x60
	ds_read_b64_tr_b16 v[98:99], v166 offset:0x1260
	ds_read_b64_tr_b16 v[100:101], v166 offset:0x2460
	ds_read_b64_tr_b16 v[102:103], v166 offset:0x3660
	s_waitcnt lgkmcnt(8)
	v_mfma_f32_16x16x32_bf16 v[52:55], v[104:107], v[80:83], v[52:55]
	v_mfma_f32_16x16x32_bf16 v[20:23], v[104:107], v[88:91], v[20:23]
	v_mfma_f32_16x16x32_bf16 v[52:55], v[108:111], v[84:87], v[52:55]
	v_mfma_f32_16x16x32_bf16 v[20:23], v[108:111], v[92:95], v[20:23]
	ds_read_b64_tr_b16 v[104:105], v166 offset:0x80
	ds_read_b64_tr_b16 v[106:107], v166 offset:0x1280
	ds_read_b64_tr_b16 v[108:109], v166 offset:0x2480
	ds_read_b64_tr_b16 v[110:111], v166 offset:0x3680
	s_waitcnt lgkmcnt(8)
	v_mfma_f32_16x16x32_bf16 v[56:59], v[158:161], v[80:83], v[56:59]
	v_mfma_f32_16x16x32_bf16 v[24:27], v[158:161], v[88:91], v[24:27]
	v_mfma_f32_16x16x32_bf16 v[56:59], v[162:165], v[84:87], v[56:59]
	v_mfma_f32_16x16x32_bf16 v[24:27], v[162:165], v[92:95], v[24:27]
	ds_read_b64_tr_b16 v[158:159], v166 offset:0xa0
	ds_read_b64_tr_b16 v[160:161], v166 offset:0x12a0
	ds_read_b64_tr_b16 v[162:163], v166 offset:0x24a0
	ds_read_b64_tr_b16 v[164:165], v166 offset:0x36a0
	s_waitcnt lgkmcnt(8)
	v_mfma_f32_16x16x32_bf16 v[60:63], v[96:99], v[80:83], v[60:63]
	v_mfma_f32_16x16x32_bf16 v[28:31], v[96:99], v[88:91], v[28:31]
	v_mfma_f32_16x16x32_bf16 v[60:63], v[100:103], v[84:87], v[60:63]
	v_mfma_f32_16x16x32_bf16 v[28:31], v[100:103], v[92:95], v[28:31]
	ds_read_b64_tr_b16 v[96:97], v166 offset:0xc0
	ds_read_b64_tr_b16 v[98:99], v166 offset:0x12c0
	ds_read_b64_tr_b16 v[100:101], v166 offset:0x24c0
	ds_read_b64_tr_b16 v[102:103], v166 offset:0x36c0
	s_waitcnt lgkmcnt(8)
	v_mfma_f32_16x16x32_bf16 v[68:71], v[104:107], v[80:83], v[68:71]
	v_mfma_f32_16x16x32_bf16 v[32:35], v[104:107], v[88:91], v[32:35]
	v_mfma_f32_16x16x32_bf16 v[68:71], v[108:111], v[84:87], v[68:71]
	v_mfma_f32_16x16x32_bf16 v[32:35], v[108:111], v[92:95], v[32:35]
	ds_read_b64_tr_b16 v[104:105], v166 offset:0xe0
	ds_read_b64_tr_b16 v[106:107], v166 offset:0x12e0
	ds_read_b64_tr_b16 v[108:109], v166 offset:0x24e0
	ds_read_b64_tr_b16 v[110:111], v166 offset:0x36e0
	s_waitcnt lgkmcnt(8)
	v_mfma_f32_16x16x32_bf16 v[76:79], v[158:161], v[80:83], v[76:79]
	s_waitcnt lgkmcnt(4)
	v_mfma_f32_16x16x32_bf16 v[36:39], v[158:161], v[88:91], v[36:39]
	v_mfma_f32_16x16x32_bf16 v[76:79], v[162:165], v[84:87], v[76:79]
	v_mfma_f32_16x16x32_bf16 v[36:39], v[162:165], v[92:95], v[36:39]
	v_mfma_f32_16x16x32_bf16 v[64:67], v[96:99], v[80:83], v[64:67]
	s_waitcnt lgkmcnt(0)
	v_mfma_f32_16x16x32_bf16 v[40:43], v[96:99], v[88:91], v[40:43]
	v_mfma_f32_16x16x32_bf16 v[64:67], v[100:103], v[84:87], v[64:67]
	v_mfma_f32_16x16x32_bf16 v[40:43], v[100:103], v[92:95], v[40:43]
	v_mfma_f32_16x16x32_bf16 v[72:75], v[104:107], v[80:83], v[72:75]
	v_mfma_f32_16x16x32_bf16 v[44:47], v[104:107], v[88:91], v[44:47]
	v_mfma_f32_16x16x32_bf16 v[72:75], v[108:111], v[84:87], v[72:75]
	v_mfma_f32_16x16x32_bf16 v[44:47], v[108:111], v[92:95], v[44:47]
	s_setprio 0
	s_add_i32 s36, s36, 1
	s_add_i32 s37, s37, -1
	s_add_i32 s6, s5, s36
	v_add_u32_e32 v154, 64, v154
	v_subrev_u32_e32 v155, 64, v155
	s_cmp_eq_u32 s6, 1
	v_subrev_u32_e32 v156, 64, v156
	s_cbranch_scc1 .LBB0_1437

; __device__ __forceinline__ float xmax16(float v) { float a = v, b = v; PL_SWAP16(a, b); return fmaxf(a, b); }
; __device__ __forceinline__ float xmax32(float v) { float a = v, b = v; PL_SWAP32(a, b); return fmaxf(a, b); }
; template <bool WITH_O, class G> __device__ __forceinline__ void online_smc(f32x4 (&s)[4], G& g, const float ref) {
;     float mx = s[0][0];
; #pragma unroll
;     for (int T_ = 0; T_ < 4; ++T_)
; #pragma unroll
;         for (int i = 0; i < 4; ++i) mx = fmaxf(mx, s[T_][i]);
;     const float t = mx + ref;
;     if (!__all(t <= g.m + SM_THR)) {
;         const float mr = xmax32(xmax16(t));
;         const float mn = fmaxf(g.m, mr); const float al = __builtin_amdgcn_exp2f(g.m - mn); g.m = mn; g.l *= al;
;         if (WITH_O) {
; #pragma unroll
;             for (int dt = 0; dt < 8; ++dt) g.o[dt] = g.o[dt] * al; }
;         const float d = ref - mn;
; #pragma unroll
;         for (int T_ = 0; T_ < 4; ++T_)
; #pragma unroll
;             for (int i = 0; i < 4; ++i) s[T_][i] += d;
;     }
.LBB0_1491:
	s_nop 3
	v_max_f32_e32 v130, v100, v101
	v_max3_f32 v130, v130, v102, v103
	v_max3_f32 v130, v130, v108, v109
	v_max3_f32 v130, v130, v110, v111
	v_max3_f32 v130, v130, v104, v105
	v_max3_f32 v130, v130, v106, v107
	v_max3_f32 v130, v130, v96, v97
	v_max3_f32 v130, v130, v98, v99
	v_pk_add_f32 v[138:139], v[136:137], v[130:131]
	s_nop 0
	v_cmp_le_f32_e32 vcc, v138, v139
	s_cmp_eq_u64 vcc, exec
	s_cbranch_scc1 .LBB0_1493
	v_mov_b32_e32 v130, v138
	s_nop 1
	v_permlane16_swap_b32 v130, v138
	s_nop 0
	v_max_f32_e32 v138, v138, v138
	v_max_f32_e32 v130, v130, v130
	v_max_f32_e32 v130, v130, v138
	v_mov_b32_e32 v138, v130
	s_nop 1
	v_permlane32_swap_b32 v138, v130
	s_nop 0
	v_max3_f32 v138, v137, v138, v130
	v_sub_f32_e32 v130, v137, v138
	v_exp_f32_e32 v130, v130
	v_mov_b32_e32 v137, v138
	v_mul_f32_e32 v152, v152, v130
	v_pk_mul_f32 v[50:51], v[50:51], v[130:131] op_sel_hi:[1,0]
	v_pk_mul_f32 v[48:49], v[48:49], v[130:131] op_sel_hi:[1,0]
	v_pk_mul_f32 v[54:55], v[54:55], v[130:131] op_sel_hi:[1,0]
	v_pk_mul_f32 v[52:53], v[52:53], v[130:131] op_sel_hi:[1,0]
	v_pk_mul_f32 v[58:59], v[58:59], v[130:131] op_sel_hi:[1,0]
	v_pk_mul_f32 v[56:57], v[56:57], v[130:131] op_sel_hi:[1,0]
	v_pk_mul_f32 v[62:63], v[62:63], v[130:131] op_sel_hi:[1,0]
	v_pk_mul_f32 v[60:61], v[60:61], v[130:131] op_sel_hi:[1,0]
	v_pk_mul_f32 v[70:71], v[70:71], v[130:131] op_sel_hi:[1,0]
	v_pk_mul_f32 v[68:69], v[68:69], v[130:131] op_sel_hi:[1,0]
	v_pk_mul_f32 v[78:79], v[78:79], v[130:131] op_sel_hi:[1,0]
	v_pk_mul_f32 v[76:77], v[76:77], v[130:131] op_sel_hi:[1,0]
	v_pk_mul_f32 v[66:67], v[66:67], v[130:131] op_sel_hi:[1,0]
	v_pk_mul_f32 v[64:65], v[64:65], v[130:131] op_sel_hi:[1,0]
	v_pk_mul_f32 v[74:75], v[74:75], v[130:131] op_sel_hi:[1,0]
	v_pk_mul_f32 v[72:73], v[72:73], v[130:131] op_sel_hi:[1,0]
	v_sub_f32_e32 v130, v136, v138
	v_pk_add_f32 v[100:101], v[100:101], v[130:131] op_sel_hi:[1,0]
	v_pk_add_f32 v[102:103], v[102:103], v[130:131] op_sel_hi:[1,0]
	v_pk_add_f32 v[108:109], v[108:109], v[130:131] op_sel_hi:[1,0]
	v_pk_add_f32 v[110:111], v[110:111], v[130:131] op_sel_hi:[1,0]
	v_pk_add_f32 v[104:105], v[104:105], v[130:131] op_sel_hi:[1,0]
	v_pk_add_f32 v[106:107], v[106:107], v[130:131] op_sel_hi:[1,0]
	v_pk_add_f32 v[96:97], v[96:97], v[130:131] op_sel_hi:[1,0]
	v_pk_add_f32 v[98:99], v[98:99], v[130:131] op_sel_hi:[1,0]
.LBB0_1493:
	v_max_f32_e32 v130, v92, v93
	v_max3_f32 v130, v130, v94, v95
	v_max3_f32 v130, v130, v88, v89
	v_max3_f32 v130, v130, v90, v91
	v_max3_f32 v130, v130, v80, v81
	v_max3_f32 v130, v130, v82, v83
	v_max3_f32 v130, v130, v84, v85
	v_max3_f32 v130, v130, v86, v87
	v_pk_add_f32 v[138:139], v[134:135], v[130:131]
	s_nop 0
	v_cmp_le_f32_e32 vcc, v138, v139
	s_cmp_eq_u64 vcc, exec
	s_cbranch_scc1 .LBB0_1470
	v_mov_b32_e32 v130, v138
	s_nop 1
	v_permlane16_swap_b32 v138, v130
	s_nop 0
	v_max_f32_e32 v130, v130, v130
	v_max_f32_e32 v136, v138, v138
	v_max_f32_e32 v130, v136, v130
	v_mov_b32_e32 v136, v130
	s_nop 1
	v_permlane32_swap_b32 v130, v136
	s_nop 0
	v_max3_f32 v136, v135, v130, v136
	v_sub_f32_e32 v130, v135, v136
	v_exp_f32_e32 v130, v130
	v_mov_b32_e32 v135, v136
	v_mul_f32_e32 v153, v153, v130
	v_pk_mul_f32 v[18:19], v[18:19], v[130:131] op_sel_hi:[1,0]
	v_pk_mul_f32 v[16:17], v[16:17], v[130:131] op_sel_hi:[1,0]
	v_pk_mul_f32 v[22:23], v[22:23], v[130:131] op_sel_hi:[1,0]
	v_pk_mul_f32 v[20:21], v[20:21], v[130:131] op_sel_hi:[1,0]
	v_pk_mul_f32 v[26:27], v[26:27], v[130:131] op_sel_hi:[1,0]
	v_pk_mul_f32 v[24:25], v[24:25], v[130:131] op_sel_hi:[1,0]
	v_pk_mul_f32 v[30:31], v[30:31], v[130:131] op_sel_hi:[1,0]
	v_pk_mul_f32 v[28:29], v[28:29], v[130:131] op_sel_hi:[1,0]
	v_pk_mul_f32 v[34:35], v[34:35], v[130:131] op_sel_hi:[1,0]
	v_pk_mul_f32 v[32:33], v[32:33], v[130:131] op_sel_hi:[1,0]
	v_pk_mul_f32 v[38:39], v[38:39], v[130:131] op_sel_hi:[1,0]
	v_pk_mul_f32 v[36:37], v[36:37], v[130:131] op_sel_hi:[1,0]
	v_pk_mul_f32 v[42:43], v[42:43], v[130:131] op_sel_hi:[1,0]
	v_pk_mul_f32 v[40:41], v[40:41], v[130:131] op_sel_hi:[1,0]
	v_pk_mul_f32 v[46:47], v[46:47], v[130:131] op_sel_hi:[1,0]
	v_pk_mul_f32 v[44:45], v[44:45], v[130:131] op_sel_hi:[1,0]
	v_sub_f32_e32 v130, v134, v136
	v_pk_add_f32 v[92:93], v[92:93], v[130:131] op_sel_hi:[1,0]
	v_pk_add_f32 v[94:95], v[94:95], v[130:131] op_sel_hi:[1,0]
	v_pk_add_f32 v[88:89], v[88:89], v[130:131] op_sel_hi:[1,0]
	v_pk_add_f32 v[90:91], v[90:91], v[130:131] op_sel_hi:[1,0]
	v_pk_add_f32 v[80:81], v[80:81], v[130:131] op_sel_hi:[1,0]
	v_pk_add_f32 v[82:83], v[82:83], v[130:131] op_sel_hi:[1,0]
	v_pk_add_f32 v[84:85], v[84:85], v[130:131] op_sel_hi:[1,0]
	v_pk_add_f32 v[86:87], v[86:87], v[130:131] op_sel_hi:[1,0]
	s_branch .LBB0_1470

; #define GAS __attribute__((address_space(1)))
; __device__ __forceinline__ unsigned pk4_fp8(float a, float b, float c, float d) { unsigned w = 0u; w = __builtin_amdgcn_cvt_pk_fp8_f32(a, b, w, false); w = __builtin_amdgcn_cvt_pk_fp8_f32(c, d, w, true); return w; }
; __device__ __forceinline__ void gs8_init(GS8& g, const bf16* qrow32) {
; #pragma unroll
;     for (int i = 0; i < 4; ++i) { const u32x4 w = *(const GAS u32x4*)(qrow32 + 8 * i);
;         g.q8[2 * i] = (int)pk4_fp8(bf_lo(w.x) * 8.f, bf_hi(w.x) * 8.f, bf_lo(w.y) * 8.f, bf_hi(w.y) * 8.f); g.q8[2 * i + 1] = (int)pk4_fp8(bf_lo(w.z) * 8.f, bf_hi(w.z) * 8.f, bf_lo(w.w) * 8.f, bf_hi(w.w) * 8.f); }
; #pragma unroll
;     for (int dt = 0; dt < 8; ++dt) g.o[dt] = (f32x4){0.f, 0.f, 0.f, 0.f};
;     g.m = -1e30f; g.l = 0.f;
; }
.LBB0_1569:
	s_waitcnt vmcnt(0)
	v_lshlrev_b32_e32 v0, 16, v30
	v_mul_f32_e32 v1, 0x41000000, v0
	v_and_b32_e32 v0, 0xffff0000, v30
	v_mul_f32_e32 v30, 0x41000000, v0
	v_lshlrev_b32_e32 v0, 16, v31
	v_mul_f32_e32 v34, 0x41000000, v0
	v_mov_b32_e32 v0, v127
	v_cvt_pk_fp8_f32 v0, v1, v30
	v_and_b32_e32 v1, 0xffff0000, v31
	v_mul_f32_e32 v1, 0x41000000, v1
	s_lshr_b32 s60, s73, 4
	v_cvt_pk_fp8_f32 v0, v34, v1 op_sel:[0,0,1]
	v_lshlrev_b32_e32 v1, 16, v32
	v_mul_f32_e32 v30, 0x41000000, v1
	v_and_b32_e32 v1, 0xffff0000, v32
	v_mul_f32_e32 v31, 0x41000000, v1
	v_mov_b32_e32 v1, v127
	v_cvt_pk_fp8_f32 v1, v30, v31
	v_lshlrev_b32_e32 v32, 16, v33
	v_and_b32_e32 v31, 0xffff0000, v33
	v_mul_f32_e32 v30, 0x41000000, v32
	v_mul_f32_e32 v31, 0x41000000, v31
	v_cvt_pk_fp8_f32 v1, v30, v31 op_sel:[0,0,1]
	v_lshlrev_b32_e32 v30, 16, v2
	v_and_b32_e32 v2, 0xffff0000, v2
	v_mul_f32_e32 v30, 0x41000000, v30
	v_mul_f32_e32 v31, 0x41000000, v2
	v_mov_b32_e32 v2, v127
	v_cvt_pk_fp8_f32 v2, v30, v31
	v_lshlrev_b32_e32 v32, 16, v3
	v_and_b32_e32 v3, 0xffff0000, v3
	v_mul_f32_e32 v30, 0x41000000, v32
	v_mul_f32_e32 v3, 0x41000000, v3
	v_cvt_pk_fp8_f32 v2, v30, v3 op_sel:[0,0,1]
	v_lshlrev_b32_e32 v3, 16, v4
	v_mul_f32_e32 v30, 0x41000000, v3
	v_and_b32_e32 v3, 0xffff0000, v4
	v_mul_f32_e32 v4, 0x41000000, v3
	v_mov_b32_e32 v3, v127
	v_cvt_pk_fp8_f32 v3, v30, v4
	v_lshlrev_b32_e32 v31, 16, v5
	v_and_b32_e32 v5, 0xffff0000, v5
	v_mul_f32_e32 v4, 0x41000000, v31
	v_mul_f32_e32 v5, 0x41000000, v5
	v_cvt_pk_fp8_f32 v3, v4, v5 op_sel:[0,0,1]
	v_lshlrev_b32_e32 v4, 16, v26
	v_mul_f32_e32 v5, 0x41000000, v4
	v_and_b32_e32 v4, 0xffff0000, v26
	v_mul_f32_e32 v26, 0x41000000, v4
	v_mov_b32_e32 v4, v127
	v_cvt_pk_fp8_f32 v4, v5, v26
	v_lshlrev_b32_e32 v30, 16, v27
	v_and_b32_e32 v26, 0xffff0000, v27
	v_mul_f32_e32 v5, 0x41000000, v30
	v_mul_f32_e32 v26, 0x41000000, v26
	v_cvt_pk_fp8_f32 v4, v5, v26 op_sel:[0,0,1]
	v_lshlrev_b32_e32 v5, 16, v28
	v_mul_f32_e32 v26, 0x41000000, v5
	v_and_b32_e32 v5, 0xffff0000, v28
	v_mul_f32_e32 v27, 0x41000000, v5
	v_mov_b32_e32 v5, v127
	v_cvt_pk_fp8_f32 v5, v26, v27
	v_lshlrev_b32_e32 v28, 16, v29
	v_and_b32_e32 v27, 0xffff0000, v29
	v_mul_f32_e32 v26, 0x41000000, v28
	v_mul_f32_e32 v27, 0x41000000, v27
	v_cvt_pk_fp8_f32 v5, v26, v27 op_sel:[0,0,1]
	v_lshlrev_b32_e32 v26, 16, v6
	v_and_b32_e32 v6, 0xffff0000, v6
	v_mul_f32_e32 v26, 0x41000000, v26
	v_mul_f32_e32 v27, 0x41000000, v6
	v_mov_b32_e32 v6, v127
	v_cvt_pk_fp8_f32 v6, v26, v27
	v_lshlrev_b32_e32 v28, 16, v7
	v_and_b32_e32 v7, 0xffff0000, v7
	v_mul_f32_e32 v26, 0x41000000, v28
	v_mul_f32_e32 v7, 0x41000000, v7
	v_cvt_pk_fp8_f32 v6, v26, v7 op_sel:[0,0,1]
	v_lshlrev_b32_e32 v7, 16, v8
	v_mul_f32_e32 v26, 0x41000000, v7
	v_and_b32_e32 v7, 0xffff0000, v8
	v_mul_f32_e32 v8, 0x41000000, v7
	v_mov_b32_e32 v7, v127
	v_cvt_pk_fp8_f32 v7, v26, v8
	v_lshlrev_b32_e32 v27, 16, v9
	v_and_b32_e32 v9, 0xffff0000, v9
	v_mul_f32_e32 v8, 0x41000000, v27
	v_mul_f32_e32 v9, 0x41000000, v9
	v_cvt_pk_fp8_f32 v7, v8, v9 op_sel:[0,0,1]
	v_lshlrev_b32_e32 v8, 16, v22
	v_mul_f32_e32 v9, 0x41000000, v8
	v_and_b32_e32 v8, 0xffff0000, v22
	v_mul_f32_e32 v22, 0x41000000, v8
	v_mov_b32_e32 v8, v127
	v_cvt_pk_fp8_f32 v8, v9, v22
	v_lshlrev_b32_e32 v26, 16, v23
	v_and_b32_e32 v22, 0xffff0000, v23
	v_mul_f32_e32 v9, 0x41000000, v26
	v_mul_f32_e32 v22, 0x41000000, v22
	v_cvt_pk_fp8_f32 v8, v9, v22 op_sel:[0,0,1]
	v_lshlrev_b32_e32 v9, 16, v24
	v_mul_f32_e32 v22, 0x41000000, v9
	v_and_b32_e32 v9, 0xffff0000, v24
	v_mul_f32_e32 v23, 0x41000000, v9
	v_mov_b32_e32 v9, v127
	v_cvt_pk_fp8_f32 v9, v22, v23
	v_lshlrev_b32_e32 v24, 16, v25
	v_and_b32_e32 v23, 0xffff0000, v25
	v_mul_f32_e32 v22, 0x41000000, v24
	v_mul_f32_e32 v23, 0x41000000, v23
	v_cvt_pk_fp8_f32 v9, v22, v23 op_sel:[0,0,1]
	v_lshlrev_b32_e32 v22, 16, v10
	v_and_b32_e32 v10, 0xffff0000, v10
	v_mul_f32_e32 v22, 0x41000000, v22
	v_mul_f32_e32 v23, 0x41000000, v10
	v_mov_b32_e32 v10, v127
	v_cvt_pk_fp8_f32 v10, v22, v23
	v_lshlrev_b32_e32 v24, 16, v11
	v_and_b32_e32 v11, 0xffff0000, v11
	v_mul_f32_e32 v22, 0x41000000, v24
	v_mul_f32_e32 v11, 0x41000000, v11
; #define GAS __attribute__((address_space(1)))
; #define LAS __attribute__((address_space(3)))
; __device__ __forceinline__ unsigned pk4_fp8(float a, float b, float c, float d) { unsigned w = 0u; w = __builtin_amdgcn_cvt_pk_fp8_f32(a, b, w, false); w = __builtin_amdgcn_cvt_pk_fp8_f32(c, d, w, true); return w; }
; __device__ __forceinline__ void gs8_init(GS8& g, const bf16* qrow32) {
; #pragma unroll
;     for (int i = 0; i < 4; ++i) { const u32x4 w = *(const GAS u32x4*)(qrow32 + 8 * i);
;         g.q8[2 * i] = (int)pk4_fp8(bf_lo(w.x) * 8.f, bf_hi(w.x) * 8.f, bf_lo(w.y) * 8.f, bf_hi(w.y) * 8.f); g.q8[2 * i + 1] = (int)pk4_fp8(bf_lo(w.z) * 8.f, bf_hi(w.z) * 8.f, bf_lo(w.w) * 8.f, bf_hi(w.w) * 8.f); }
; #pragma unroll
;     for (int dt = 0; dt < 8; ++dt) g.o[dt] = (f32x4){0.f, 0.f, 0.f, 0.f};
;     g.m = -1e30f; g.l = 0.f;
; }
; __device__ __forceinline__ void cmp_phase(Frame& F) {
;     ...
;         GS8 g0, g1; gs8_init(g0, Q + qoff + 32 * kq); gs8_init(g1, Q + qoff + 4 * HD + 32 * kq);
;         const int nkt = ((4 * cur + 2) >> 6) + 1, nit = 2 * nkt;
;         const int limA = (tokA - 31) >> 4, limB = (tokA + 4 - 31) >> 4;
;         const char* Kb = KC + (size_t)bh * 1024 * HD; const char* Vb = VC + (size_t)bh * 1024 * HD * 2;
;         if (F.tid < 256) { unsigned long long mv = 0ull; if (cur < 16) mv = (F.tid <= cur) ? ~0ull : 0ull; else mv = (F.tid == 0 || F.tid == cur || F.tid == cur - 1) ? ~0ull : 0ull; Ml[F.tid] = mv; }
;         float i0 = 0.f, i1 = 0.f, carry0 = 0.f, carry1 = 0.f;
;         LAS float* impA = imp + (8 * F.wave + (c >> 2)) * 256; LAS float* impB = impA + 4 * 256;
	v_cvt_pk_fp8_f32 v10, v22, v11 op_sel:[0,0,1]
	v_lshlrev_b32_e32 v11, 16, v12
	v_mul_f32_e32 v22, 0x41000000, v11
	v_and_b32_e32 v11, 0xffff0000, v12
	v_mul_f32_e32 v12, 0x41000000, v11
	v_mov_b32_e32 v11, v127
	v_cvt_pk_fp8_f32 v11, v22, v12
	v_lshlrev_b32_e32 v23, 16, v13
	v_and_b32_e32 v13, 0xffff0000, v13
	v_mul_f32_e32 v12, 0x41000000, v23
	v_mul_f32_e32 v13, 0x41000000, v13
	v_cvt_pk_fp8_f32 v11, v12, v13 op_sel:[0,0,1]
	v_lshlrev_b32_e32 v12, 16, v18
	v_mul_f32_e32 v13, 0x41000000, v12
	v_and_b32_e32 v12, 0xffff0000, v18
	v_mul_f32_e32 v18, 0x41000000, v12
	v_mov_b32_e32 v12, v127
	v_cvt_pk_fp8_f32 v12, v13, v18
	v_lshlrev_b32_e32 v22, 16, v19
	v_and_b32_e32 v18, 0xffff0000, v19
	v_mul_f32_e32 v13, 0x41000000, v22
	v_mul_f32_e32 v18, 0x41000000, v18
	v_cvt_pk_fp8_f32 v12, v13, v18 op_sel:[0,0,1]
	v_lshlrev_b32_e32 v13, 16, v20
	v_mul_f32_e32 v18, 0x41000000, v13
	v_and_b32_e32 v13, 0xffff0000, v20
	v_mul_f32_e32 v19, 0x41000000, v13
	v_mov_b32_e32 v13, v127
	v_cvt_pk_fp8_f32 v13, v18, v19
	v_lshlrev_b32_e32 v20, 16, v21
	v_and_b32_e32 v19, 0xffff0000, v21
	v_mul_f32_e32 v18, 0x41000000, v20
	v_mul_f32_e32 v19, 0x41000000, v19
	v_cvt_pk_fp8_f32 v13, v18, v19 op_sel:[0,0,1]
	v_lshlrev_b32_e32 v18, 16, v14
	v_and_b32_e32 v14, 0xffff0000, v14
	v_mul_f32_e32 v18, 0x41000000, v18
	v_mul_f32_e32 v19, 0x41000000, v14
	v_mov_b32_e32 v14, v127
	v_cvt_pk_fp8_f32 v14, v18, v19
	v_lshlrev_b32_e32 v20, 16, v15
	v_and_b32_e32 v15, 0xffff0000, v15
	v_mul_f32_e32 v18, 0x41000000, v20
	v_mul_f32_e32 v15, 0x41000000, v15
	v_cvt_pk_fp8_f32 v14, v18, v15 op_sel:[0,0,1]
	v_lshlrev_b32_e32 v15, 16, v16
	v_mul_f32_e32 v18, 0x41000000, v15
	v_and_b32_e32 v15, 0xffff0000, v16
	v_mul_f32_e32 v16, 0x41000000, v15
	v_mov_b32_e32 v15, v127
	v_cvt_pk_fp8_f32 v15, v18, v16
	v_lshlrev_b32_e32 v19, 16, v17
	v_and_b32_e32 v17, 0xffff0000, v17
	v_mul_f32_e32 v16, 0x41000000, v19
	v_mul_f32_e32 v17, 0x41000000, v17
	v_cvt_pk_fp8_f32 v15, v16, v17 op_sel:[0,0,1]
	v_subrev_u32_e32 v16, 31, v126
	v_subrev_u32_e32 v17, 27, v126
	v_ashrrev_i32_e32 v16, 4, v16
	v_ashrrev_i32_e32 v17, 4, v17
	v_mov_b32_e32 v44, v127
	v_mov_b32_e32 v45, v127
	v_mov_b32_e32 v46, v127
	v_mov_b32_e32 v47, v127
	s_add_i32 s61, s60, 1
	s_sub_i32 s22, s36, 31
	s_lshl_b32 s78, s60, 6
	v_sub_u32_e32 v186, v116, v17
	v_add_u32_e32 v187, v119, v17
	v_add_u32_e32 v188, v119, v16
	v_sub_u32_e32 v189, v116, v16
	v_mov_b64_e32 v[40:41], v[44:45]
	v_mov_b64_e32 v[36:37], v[44:45]
	v_mov_b64_e32 v[32:33], v[44:45]
	v_mov_b64_e32 v[28:29], v[44:45]
	v_mov_b64_e32 v[24:25], v[44:45]
	v_mov_b64_e32 v[20:21], v[44:45]
	v_mov_b64_e32 v[16:17], v[44:45]
	v_mov_b64_e32 v[78:79], v[46:47]
	v_mov_b64_e32 v[74:75], v[46:47]
	v_mov_b64_e32 v[70:71], v[46:47]
	v_mov_b64_e32 v[66:67], v[46:47]
	v_mov_b64_e32 v[62:63], v[46:47]
	v_mov_b64_e32 v[58:59], v[46:47]
	v_mov_b64_e32 v[54:55], v[46:47]
	v_mov_b64_e32 v[50:51], v[46:47]
	s_mov_b32 s59, 0
	s_lshl_b32 s74, s61, 1
	s_ashr_i32 s75, s22, 4
	s_sub_i32 s76, 0, s60
	s_add_i32 s78, s78, 64
	v_mov_b32_e32 v142, v127
	v_mov_b32_e32 v113, v127
	v_mov_b32_e32 v139, 0xf149f2ca
	v_mov_b32_e32 v192, 0
	s_mov_b32 s79, 63
	s_mov_b32 s80, 0
	v_mov_b32_e32 v193, 0
	v_mov_b64_e32 v[42:43], v[46:47]
	v_mov_b64_e32 v[38:39], v[46:47]
	v_mov_b64_e32 v[34:35], v[46:47]
	v_mov_b64_e32 v[30:31], v[46:47]
	v_mov_b64_e32 v[26:27], v[46:47]
	v_mov_b64_e32 v[22:23], v[46:47]
	v_mov_b64_e32 v[18:19], v[46:47]
	v_mov_b32_e32 v190, 0
	v_mov_b32_e32 v191, 0
	v_mov_b64_e32 v[76:77], v[44:45]
	v_mov_b64_e32 v[72:73], v[44:45]
	v_mov_b64_e32 v[68:69], v[44:45]
	v_mov_b64_e32 v[64:65], v[44:45]
	v_mov_b64_e32 v[60:61], v[44:45]
	v_mov_b64_e32 v[56:57], v[44:45]
	v_mov_b64_e32 v[52:53], v[44:45]
	v_mov_b64_e32 v[48:49], v[44:45]
	v_mov_b32_e32 v141, 0xf149f2ca
	v_mov_b32_e32 v226, 0xf149f2ca
	v_mov_b32_e32 v227, 0xf149f2ca
	v_mov_b32_e32 v224, 0
	v_mov_b32_e32 v225, 0
	v_mov_b32_e32 v216, 0x80000000
	v_mov_b32_e32 v217, 0x80000000
	v_mov_b32_e32 v218, 0x80000000
	v_mov_b32_e32 v219, 0x80000000
	v_mov_b32_e32 v220, 0x80000000
	v_mov_b32_e32 v221, 0x80000000
	v_mov_b32_e32 v222, 0x80000000
	v_mov_b32_e32 v223, 0x80000000
	s_branch .LBB0_1572

; __device__ __forceinline__ float xmax16(float v) { float a = v, b = v; PL_SWAP16(a, b); return fmaxf(a, b); }
; __device__ __forceinline__ float xmax32(float v) { float a = v, b = v; PL_SWAP32(a, b); return fmaxf(a, b); }
; template <bool WITH_O, class G> __device__ __forceinline__ void online_smc(f32x4 (&s)[4], G& g, const float ref) {
;     float mx = s[0][0];
; #pragma unroll
;     for (int T_ = 0; T_ < 4; ++T_)
; #pragma unroll
;         for (int i = 0; i < 4; ++i) mx = fmaxf(mx, s[T_][i]);
;     const float t = mx + ref;
;     if (!__all(t <= g.m + SM_THR)) {
;         const float mr = xmax32(xmax16(t));
;         const float mn = fmaxf(g.m, mr); const float al = __builtin_amdgcn_exp2f(g.m - mn); g.m = mn; g.l *= al;
;         if (WITH_O) {
; #pragma unroll
;             for (int dt = 0; dt < 8; ++dt) g.o[dt] = g.o[dt] * al; }
;         const float d = ref - mn;
; #pragma unroll
;         for (int T_ = 0; T_ < 4; ++T_)
; #pragma unroll
;             for (int i = 0; i < 4; ++i) s[T_][i] += d;
;     }
.LBB0_1579:
	s_mov_b64 s[22:23], -1
	s_and_b64 vcc, exec, s[56:57]
	s_cbranch_vccz .LBB0_1585
	s_nop 0
	v_max_f32_e32 v134, v108, v109
	v_max3_f32 v134, v134, v110, v111
	v_max3_f32 v134, v134, v104, v105
	v_max3_f32 v134, v134, v106, v107
	v_max3_f32 v134, v134, v100, v101
	v_max3_f32 v134, v134, v102, v103
	v_max3_f32 v134, v134, v96, v97
	v_max3_f32 v134, v134, v98, v99
	v_add_f32_e32 v158, v224, v134
	v_cmp_le_f32_e32 vcc, v158, v226
	s_cmp_eq_u64 vcc, exec
	s_cbranch_scc1 .LBB0_1582
	v_mov_b32_e32 v134, v158
	s_nop 1
	v_permlane16_swap_b32 v158, v134
	v_max_f32_e32 v134, v134, v134
	v_max_f32_e32 v144, v158, v158
	v_max_f32_e32 v134, v144, v134
	v_mov_b32_e32 v144, v134
	s_nop 1
	v_permlane32_swap_b32 v134, v144
	v_max3_f32 v194, v141, v134, v144
	v_sub_f32_e32 v134, v141, v194
	v_exp_f32_e32 v134, v134
	v_sub_f32_e32 v144, v224, v194
	v_mul_f32_e32 v191, v191, v134
	v_mov_b32_e32 v141, v194
	v_add_f32_e32 v226, v194, v135
	v_cmp_ngt_f32_e32 vcc, s68, v141
	v_add_f32_e32 v96, v96, v144
	v_add_f32_e32 v97, v97, v144
	v_add_f32_e32 v98, v98, v144
	v_add_f32_e32 v99, v99, v144
	v_add_f32_e32 v100, v100, v144
	v_add_f32_e32 v101, v101, v144
	v_add_f32_e32 v102, v102, v144
	v_add_f32_e32 v103, v103, v144
	v_add_f32_e32 v104, v104, v144
	v_add_f32_e32 v105, v105, v144
	v_add_f32_e32 v106, v106, v144
	v_add_f32_e32 v107, v107, v144
	v_add_f32_e32 v108, v108, v144
	v_add_f32_e32 v109, v109, v144
	v_add_f32_e32 v110, v110, v144
	v_add_f32_e32 v111, v111, v144
	v_cndmask_b32_e32 v224, 0, v141, vcc
	v_xor_b32_e32 v216, 0x80000000, v224
	v_mov_b32_e32 v217, v216
	v_mov_b32_e32 v218, v216
	v_mov_b32_e32 v219, v216
.LBB0_1582:
	v_max_f32_e32 v134, v88, v89
	v_max3_f32 v134, v134, v90, v91
	v_max3_f32 v134, v134, v84, v85
	v_max3_f32 v134, v134, v86, v87
	v_max3_f32 v134, v134, v80, v81
	v_max3_f32 v134, v134, v82, v83
	v_max3_f32 v134, v134, v92, v93
	v_max3_f32 v134, v134, v94, v95
	v_add_f32_e32 v170, v225, v134
	v_cmp_le_f32_e32 vcc, v170, v227
	s_cmp_eq_u64 vcc, exec
	s_cbranch_scc1 .LBB0_1584
	v_mov_b32_e32 v134, v170
	s_nop 1
	v_permlane16_swap_b32 v170, v134
	v_max_f32_e32 v134, v134, v134
	v_max_f32_e32 v144, v170, v170
	v_max_f32_e32 v134, v144, v134
	v_mov_b32_e32 v144, v134
	s_nop 1
	v_permlane32_swap_b32 v134, v144
	v_max3_f32 v134, v139, v134, v144
	v_sub_f32_e32 v144, v139, v134
	v_exp_f32_e32 v144, v144
	v_sub_f32_e32 v138, v225, v134
	v_mul_f32_e32 v190, v190, v144
	v_mov_b32_e32 v139, v134
	v_add_f32_e32 v227, v134, v135
	v_cmp_ngt_f32_e32 vcc, s68, v139
	v_add_f32_e32 v80, v80, v138
	v_add_f32_e32 v81, v81, v138
	v_add_f32_e32 v82, v82, v138
	v_add_f32_e32 v83, v83, v138
	v_add_f32_e32 v84, v84, v138
	v_add_f32_e32 v85, v85, v138
	v_add_f32_e32 v86, v86, v138
	v_add_f32_e32 v87, v87, v138
	v_add_f32_e32 v88, v88, v138
	v_add_f32_e32 v89, v89, v138
	v_add_f32_e32 v90, v90, v138
	v_add_f32_e32 v91, v91, v138
	v_add_f32_e32 v92, v92, v138
	v_add_f32_e32 v93, v93, v138
	v_add_f32_e32 v94, v94, v138
	v_add_f32_e32 v95, v95, v138
	v_cndmask_b32_e32 v225, 0, v139, vcc
	v_xor_b32_e32 v220, 0x80000000, v225
	v_mov_b32_e32 v221, v220
	v_mov_b32_e32 v222, v220
	v_mov_b32_e32 v223, v220

; #define LAS __attribute__((address_space(3)))
; __device__ __forceinline__ unsigned lds_addr(const LAS void* p) { return (unsigned)(size_t)p; }
; __device__ __forceinline__ void imp_accum(const f32x4 (&s)[4], float& carry, LAS float* impt  , int jb, int c, int q4, int lane) {
;     float rot[4];
; #pragma unroll
;     for (int T_ = 0; T_ < 4; ++T_) rot[T_] = __shfl(s[T_][3], (lane + 48) & 63);
; #pragma unroll
;     for (int T_ = 0; T_ < 4; ++T_) { const float prev = (q4 == 0) ? (T_ == 0 ? carry : rot[T_ == 0 ? 0 : T_ - 1]) : rot[T_];
;         float v = (s[T_][0] + s[T_][1]) + (s[T_][2] + s[T_][3]) + prev;
;         v += __builtin_bit_cast(float, __builtin_amdgcn_mov_dpp(__builtin_bit_cast(int, v), 0xB1, 0xF, 0xF, true));
;         v += __builtin_bit_cast(float, __builtin_amdgcn_mov_dpp(__builtin_bit_cast(int, v), 0x4E, 0xF, 0xF, true));
;         if ((c & 3) == 0) impt[jb + 4 * T_ + q4] = v; }
;     carry = rot[3];
; }
; __device__ __forceinline__ void cmp_phase(Frame& F) {
;     ...
; #pragma unroll
;                 for (int T_ = 0; T_ < 4; ++T_)
; #pragma unroll
;                     for (int q = 0; q < 4; ++q) { s0[T_][q] = __builtin_amdgcn_exp2f(s0[T_][q]); s1[T_][q] = __builtin_amdgcn_exp2f(s1[T_][q]); }
;                 imp_accum(s0, carry0, impA, kt * 16, c, kq, lane); imp_accum(s1, carry1, impB, kt * 16, c, kq, lane);
;                 pv_tile<2>(g0, g1, s0, s1, lds_addr(sb + K8TB) + vlane);
.LBB0_1585:
	s_and_b64 vcc, exec, s[22:23]
	s_cbranch_vccz .LBB0_1570
	v_exp_f32_e32 v138, v109
	v_exp_f32_e32 v109, v110
	v_exp_f32_e32 v110, v111
	v_exp_f32_e32 v134, v108
	v_exp_f32_e32 v108, v107
	v_exp_f32_e32 v107, v103
	v_exp_f32_e32 v103, v99
	ds_bpermute_b32 v146, v183, v110
	ds_bpermute_b32 v145, v183, v108
	ds_bpermute_b32 v144, v183, v107
	ds_bpermute_b32 v99, v183, v103
	v_add_f32_e32 v147, v134, v138
	v_add_f32_e32 v148, v109, v110
	s_waitcnt lgkmcnt(0)
	v_cndmask_b32_e64 v196, v146, v193, s[2:3]
	v_add_f32_e32 v147, v147, v148
	v_add_f32_e32 v196, v147, v196
	s_add_i32 s22, s79, s48
	v_add_u32_e32 v111, s22, v117
	v_exp_f32_e32 v140, v104
	v_exp_f32_e32 v105, v105
	v_exp_f32_e32 v104, v106
	v_cndmask_b32_e64 v197, v145, v146, s[2:3]
	v_add_f32_e32 v146, v140, v105
	v_add_f32_e32 v147, v104, v108
	v_add_f32_e32 v146, v146, v147
	v_add_f32_e32 v197, v146, v197
	v_exp_f32_e32 v106, v100
	v_exp_f32_e32 v101, v101
	v_exp_f32_e32 v100, v102
	v_cndmask_b32_e64 v198, v144, v145, s[2:3]
	v_add_f32_e32 v145, v106, v101
	v_add_f32_e32 v146, v100, v107
	v_add_f32_e32 v145, v145, v146
	v_add_f32_e32 v198, v145, v198
	v_exp_f32_e32 v102, v96
	v_exp_f32_e32 v97, v97
	v_exp_f32_e32 v96, v98
	v_cndmask_b32_e64 v199, v99, v144, s[2:3]
	v_add_f32_e32 v144, v102, v97
	v_add_f32_e32 v145, v96, v103
	v_add_f32_e32 v144, v144, v145
	v_add_f32_e32 v199, v144, v199
	v_exp_f32_e32 v91, v91
	v_exp_f32_e32 v98, v88
	v_exp_f32_e32 v144, v89
	v_exp_f32_e32 v89, v87
	v_exp_f32_e32 v88, v83
	v_exp_f32_e32 v87, v95
	ds_bpermute_b32 v147, v183, v91
	v_exp_f32_e32 v90, v90
	ds_bpermute_b32 v146, v183, v89
	ds_bpermute_b32 v145, v183, v88
	ds_bpermute_b32 v83, v183, v87
	v_add_f32_e32 v148, v98, v144
	v_add_f32_e32 v149, v90, v91
	s_waitcnt lgkmcnt(0)
	v_cndmask_b32_e64 v200, v147, v192, s[2:3]
	v_add_f32_e32 v148, v148, v149
	v_add_f32_e32 v200, v148, v200
	v_exp_f32_e32 v95, v84
	v_exp_f32_e32 v85, v85
	v_exp_f32_e32 v84, v86
	v_cndmask_b32_e64 v201, v146, v147, s[2:3]
	v_add_f32_e32 v147, v95, v85
	v_add_f32_e32 v148, v84, v89
	v_add_f32_e32 v147, v147, v148
	v_add_f32_e32 v201, v147, v201
	v_exp_f32_e32 v86, v80
	v_exp_f32_e32 v81, v81
	v_exp_f32_e32 v80, v82
	v_cndmask_b32_e64 v202, v145, v146, s[2:3]
	v_add_f32_e32 v146, v86, v81
	v_add_f32_e32 v147, v80, v88
	v_add_f32_e32 v146, v146, v147
	v_add_f32_e32 v202, v146, v202
	v_exp_f32_e32 v92, v92
	v_exp_f32_e32 v93, v93
	v_exp_f32_e32 v82, v94
	v_cndmask_b32_e64 v203, v83, v145, s[2:3]
	v_add_f32_e32 v145, v92, v93
	v_add_f32_e32 v146, v82, v87
	v_add_f32_e32 v145, v145, v146
	v_add_f32_e32 v203, v145, v203
	v_add_f32_dpp v196, v196, v196 quad_perm:[1,0,3,2] row_mask:0xf bank_mask:0xf bound_ctrl:1
	v_add_f32_dpp v197, v197, v197 quad_perm:[1,0,3,2] row_mask:0xf bank_mask:0xf bound_ctrl:1
	v_add_f32_dpp v198, v198, v198 quad_perm:[1,0,3,2] row_mask:0xf bank_mask:0xf bound_ctrl:1
	v_add_f32_dpp v199, v199, v199 quad_perm:[1,0,3,2] row_mask:0xf bank_mask:0xf bound_ctrl:1
	v_add_f32_dpp v200, v200, v200 quad_perm:[1,0,3,2] row_mask:0xf bank_mask:0xf bound_ctrl:1
	v_add_f32_dpp v201, v201, v201 quad_perm:[1,0,3,2] row_mask:0xf bank_mask:0xf bound_ctrl:1
	v_add_f32_dpp v202, v202, v202 quad_perm:[1,0,3,2] row_mask:0xf bank_mask:0xf bound_ctrl:1
	v_add_f32_dpp v203, v203, v203 quad_perm:[1,0,3,2] row_mask:0xf bank_mask:0xf bound_ctrl:1
	v_add_f32_dpp v196, v196, v196 quad_perm:[2,3,0,1] row_mask:0xf bank_mask:0xf bound_ctrl:1
	v_add_f32_dpp v197, v197, v197 quad_perm:[2,3,0,1] row_mask:0xf bank_mask:0xf bound_ctrl:1
	v_add_f32_dpp v198, v198, v198 quad_perm:[2,3,0,1] row_mask:0xf bank_mask:0xf bound_ctrl:1
	v_add_f32_dpp v199, v199, v199 quad_perm:[2,3,0,1] row_mask:0xf bank_mask:0xf bound_ctrl:1
	v_add_f32_dpp v200, v200, v200 quad_perm:[2,3,0,1] row_mask:0xf bank_mask:0xf bound_ctrl:1
	v_add_f32_dpp v201, v201, v201 quad_perm:[2,3,0,1] row_mask:0xf bank_mask:0xf bound_ctrl:1
	v_add_f32_dpp v202, v202, v202 quad_perm:[2,3,0,1] row_mask:0xf bank_mask:0xf bound_ctrl:1
	v_add_f32_dpp v203, v203, v203 quad_perm:[2,3,0,1] row_mask:0xf bank_mask:0xf bound_ctrl:1
	s_and_saveexec_b64 s[22:23], s[4:5]
	v_add_u32_e32 v212, 0x117c1, v111
	ds_write_b32 v212, v196
	ds_write_b32 v212, v197 offset:16
	ds_write_b32 v212, v198 offset:32
	ds_write_b32 v212, v199 offset:48
	ds_write_b32 v212, v200 offset:4096
	ds_write_b32 v212, v201 offset:4112
	ds_write_b32 v212, v202 offset:4128
	ds_write_b32 v212, v203 offset:4144
	s_or_b64 exec, exec, s[22:23]
	s_addk_i32 s37, 0x2400
	v_add_u32_e32 v145, s37, v173
	v_cvt_pk_bf16_f32 v146, v134, v138
	v_cvt_pk_bf16_f32 v147, v109, v110
	v_cvt_pk_bf16_f32 v148, v140, v105
	v_cvt_pk_bf16_f32 v149, v104, v108
	v_cvt_pk_bf16_f32 v104, v106, v101
	v_cvt_pk_bf16_f32 v105, v100, v107
	v_cvt_pk_bf16_f32 v106, v102, v97
	v_cvt_pk_bf16_f32 v107, v96, v103
	v_cvt_pk_bf16_f32 v100, v98, v144
	v_cvt_pk_bf16_f32 v101, v90, v91
	v_cvt_pk_bf16_f32 v102, v95, v85
	v_cvt_pk_bf16_f32 v103, v84, v89
	v_cvt_pk_bf16_f32 v84, v86, v81
	v_cvt_pk_bf16_f32 v85, v80, v88
	v_cvt_pk_bf16_f32 v86, v92, v93
	v_cvt_pk_bf16_f32 v87, v82, v87
	ds_read_b64_tr_b16 v[88:89], v145 offset:0
	ds_read_b64_tr_b16 v[90:91], v145 offset:0x1200
	ds_read_b64_tr_b16 v[92:93], v145 offset:0x2400
	ds_read_b64_tr_b16 v[94:95], v145 offset:0x3600
	ds_read_b64_tr_b16 v[108:109], v145 offset:32
	ds_read_b64_tr_b16 v[110:111], v145 offset:0x1220
	ds_read_b64_tr_b16 v[150:151], v145 offset:0x2420
	ds_read_b64_tr_b16 v[152:153], v145 offset:0x3620
	ds_read_b64_tr_b16 v[154:155], v145 offset:64
	ds_read_b64_tr_b16 v[156:157], v145 offset:0x1240
	ds_read_b64_tr_b16 v[158:159], v145 offset:0x2440
	ds_read_b64_tr_b16 v[160:161], v145 offset:0x3640
	s_setprio 1
	s_waitcnt lgkmcnt(8)
; #define SBAR() __builtin_amdgcn_sched_barrier(0)
; __device__ __forceinline__ bf16x8 ppack(const f32x4 a, const f32x4 b) { const u32x4 w = pack8f(a, b); return __builtin_bit_cast(bf16x8, w); }
; #define PV_RD(dt) do { TRRD(r[dt][0], vb, (dt) * 32); TRRD(r[dt][1], vb, (dt) * 32 + 4608); TRRD(r[dt][2], vb, (dt) * 32 + 9216); TRRD(r[dt][3], vb, (dt) * 32 + 9216 + 4608); } while (0)
; #define PV_W(n) asm volatile("s_waitcnt lgkmcnt(" #n ")" ::: "memory"); SBAR()
; template <int NG, class G> __device__ __forceinline__ void pv_tile(G& g0, G& g1, const f32x4 (&s0)[4], const f32x4 (&s1)[4], unsigned vb) {
;     const bf16x8 pa0 = ppack(s0[0], s0[1]), pa1 = ppack(s0[2], s0[3]);
;     bf16x8 pb0 = pa0, pb1 = pa1; if (NG == 2) { pb0 = ppack(s1[0], s1[1]); pb1 = ppack(s1[2], s1[3]); }
;     s16x4 r[8][4];
;     ...
;     PV_RD(0); PV_RD(1); PV_RD(2);
;     __builtin_amdgcn_s_setprio(1);
;     PV_W(8); PV_MM(0); SBAR(); PV_RD(3);
;     PV_W(8); PV_MM(1); SBAR(); PV_RD(4);
;     PV_W(8); PV_MM(2); SBAR(); PV_RD(5);
;     PV_W(8); PV_MM(3); SBAR(); PV_RD(6);
;     PV_W(8); PV_MM(4); SBAR(); PV_RD(7);
;     PV_W(8); PV_MM(5); PV_W(4); PV_MM(6); PV_W(0); PV_MM(7);
;     __builtin_amdgcn_s_setprio(0);
; __device__ __forceinline__ void imp_accum(const f32x4 (&s)[4], float& carry, LAS float* impt  , int jb, int c, int q4, int lane) {
;     ...
;     carry = rot[3];
	v_mfma_f32_16x16x32_bf16 v[76:79], v[88:91], v[146:149], v[76:79]
	v_mfma_f32_16x16x32_bf16 v[44:47], v[88:91], v[100:103], v[44:47]
	v_mfma_f32_16x16x32_bf16 v[76:79], v[92:95], v[104:107], v[76:79]
	v_mfma_f32_16x16x32_bf16 v[44:47], v[92:95], v[84:87], v[44:47]
	ds_read_b64_tr_b16 v[88:89], v145 offset:0x60
	ds_read_b64_tr_b16 v[90:91], v145 offset:0x1260
	ds_read_b64_tr_b16 v[92:93], v145 offset:0x2460
	ds_read_b64_tr_b16 v[94:95], v145 offset:0x3660
	s_waitcnt lgkmcnt(8)
	v_mfma_f32_16x16x32_bf16 v[72:75], v[108:111], v[146:149], v[72:75]
	v_mfma_f32_16x16x32_bf16 v[40:43], v[108:111], v[100:103], v[40:43]
	v_mfma_f32_16x16x32_bf16 v[72:75], v[150:153], v[104:107], v[72:75]
	v_mfma_f32_16x16x32_bf16 v[40:43], v[150:153], v[84:87], v[40:43]
	ds_read_b64_tr_b16 v[108:109], v145 offset:0x80
	ds_read_b64_tr_b16 v[110:111], v145 offset:0x1280
	ds_read_b64_tr_b16 v[150:151], v145 offset:0x2480
	ds_read_b64_tr_b16 v[152:153], v145 offset:0x3680
	s_waitcnt lgkmcnt(8)
	v_mfma_f32_16x16x32_bf16 v[68:71], v[154:157], v[146:149], v[68:71]
	v_mfma_f32_16x16x32_bf16 v[36:39], v[154:157], v[100:103], v[36:39]
	v_mfma_f32_16x16x32_bf16 v[68:71], v[158:161], v[104:107], v[68:71]
	v_mfma_f32_16x16x32_bf16 v[36:39], v[158:161], v[84:87], v[36:39]
	ds_read_b64_tr_b16 v[154:155], v145 offset:0xa0
	ds_read_b64_tr_b16 v[156:157], v145 offset:0x12a0
	ds_read_b64_tr_b16 v[158:159], v145 offset:0x24a0
	ds_read_b64_tr_b16 v[160:161], v145 offset:0x36a0
	s_waitcnt lgkmcnt(8)
	v_mfma_f32_16x16x32_bf16 v[64:67], v[88:91], v[146:149], v[64:67]
	v_mfma_f32_16x16x32_bf16 v[32:35], v[88:91], v[100:103], v[32:35]
	v_mfma_f32_16x16x32_bf16 v[64:67], v[92:95], v[104:107], v[64:67]
	v_mfma_f32_16x16x32_bf16 v[32:35], v[92:95], v[84:87], v[32:35]
	ds_read_b64_tr_b16 v[88:89], v145 offset:0xc0
	ds_read_b64_tr_b16 v[90:91], v145 offset:0x12c0
	ds_read_b64_tr_b16 v[92:93], v145 offset:0x24c0
	ds_read_b64_tr_b16 v[94:95], v145 offset:0x36c0
	s_waitcnt lgkmcnt(8)
	v_mfma_f32_16x16x32_bf16 v[60:63], v[108:111], v[146:149], v[60:63]
	v_mfma_f32_16x16x32_bf16 v[28:31], v[108:111], v[100:103], v[28:31]
	v_mfma_f32_16x16x32_bf16 v[60:63], v[150:153], v[104:107], v[60:63]
	v_mfma_f32_16x16x32_bf16 v[28:31], v[150:153], v[84:87], v[28:31]
	ds_read_b64_tr_b16 v[108:109], v145 offset:0xe0
	ds_read_b64_tr_b16 v[110:111], v145 offset:0x12e0
	ds_read_b64_tr_b16 v[150:151], v145 offset:0x24e0
	ds_read_b64_tr_b16 v[152:153], v145 offset:0x36e0
	s_waitcnt lgkmcnt(8)
	v_mfma_f32_16x16x32_bf16 v[56:59], v[154:157], v[146:149], v[56:59]
	s_waitcnt lgkmcnt(4)
	v_mfma_f32_16x16x32_bf16 v[24:27], v[154:157], v[100:103], v[24:27]
	v_mfma_f32_16x16x32_bf16 v[56:59], v[158:161], v[104:107], v[56:59]
	v_mfma_f32_16x16x32_bf16 v[24:27], v[158:161], v[84:87], v[24:27]
	v_mfma_f32_16x16x32_bf16 v[52:55], v[88:91], v[146:149], v[52:55]
	s_waitcnt lgkmcnt(0)
	v_mfma_f32_16x16x32_bf16 v[20:23], v[88:91], v[100:103], v[20:23]
	v_mfma_f32_16x16x32_bf16 v[52:55], v[92:95], v[104:107], v[52:55]
	v_mfma_f32_16x16x32_bf16 v[20:23], v[92:95], v[84:87], v[20:23]
	v_mfma_f32_16x16x32_bf16 v[48:51], v[108:111], v[146:149], v[48:51]
	v_mfma_f32_16x16x32_bf16 v[16:19], v[108:111], v[100:103], v[16:19]
	v_mfma_f32_16x16x32_bf16 v[48:51], v[150:153], v[104:107], v[48:51]
	v_mfma_f32_16x16x32_bf16 v[16:19], v[150:153], v[84:87], v[16:19]
	s_setprio 0
	v_mov_b32_e32 v192, v83
	v_mov_b32_e32 v193, v99
	s_sub_i32 s59, s59, 64
	s_add_i32 s79, s79, 64
	s_and_b64 vcc, exec, s[54:55]
	s_cbranch_vccz .LBB0_1571
